# prep: every global load of the layer-0 weight-folding blocks issued at block start (prologue de-serialisation), consumed via v_mov
# speedup vs baseline: 1.0019x; 1.0019x over previous
.LBB0_14:
	s_andn2_saveexec_b64 s[4:5], s[18:19]
	s_cbranch_execz .LBB0_74
	s_load_dwordx2 s[24:25], s[0:1], 0x18
	s_load_dwordx2 s[26:27], s[0:1], 0x10
	s_load_dwordx4 s[28:31], s[0:1], 0x30
	s_and_b32 s22, s2, 15
	s_lshr_b32 s23, s2, 4
	s_and_b32 s23, s23, 7
	s_lshl_b32 s23, s23, 6
	v_lshrrev_b32_e32 v42, 6, v0
	v_and_b32_e32 v43, 15, v0
	v_lshl_or_b32 v42, v42, 4, v43
	v_add_u32_e32 v42, s23, v42
	s_waitcnt lgkmcnt(0)
	s_cmp_eq_u32 s22, 0
	s_cbranch_scc1 .Lw0p_first
	s_add_i32 s36, s22, -1
	s_mul_i32 s36, s36, 0x9000
	s_add_u32 s30, s30, s36
	s_addc_u32 s31, s31, 0
	v_mul_u32_u24_e32 v42, 0x48, v42
	global_load_dwordx4 v[44:47], v42, s[30:31]
	global_load_dwordx4 v[48:51], v42, s[30:31] offset:16
	global_load_dwordx4 v[52:55], v42, s[30:31] offset:32
	global_load_dwordx4 v[56:59], v42, s[30:31] offset:48
	global_load_dword v60, v42, s[30:31] offset:64
	global_load_dword v61, v42, s[30:31] offset:68
	s_branch .Lw0p_issued
.Lw0p_first:
	v_mul_u32_u24_e32 v42, 0x44, v42
	global_load_dwordx4 v[44:47], v42, s[28:29]
	global_load_dwordx4 v[48:51], v42, s[28:29] offset:16
	global_load_dwordx4 v[52:55], v42, s[28:29] offset:32
	global_load_dwordx4 v[56:59], v42, s[28:29] offset:48
	global_load_dword v60, v42, s[28:29] offset:64
.Lw0p_issued:
	s_movk_i32 s3, 0x50
	v_cmp_gt_u32_e32 vcc, s3, v0
	s_and_saveexec_b64 s[36:37], vcc
	s_mul_i32 s38, s22, 0x50
	v_add_lshl_u32 v43, v0, s38, 2
	global_load_dword v62, v43, s[24:25]
	s_mov_b64 exec, s[36:37]
	v_and_b32_e32 v43, 0xe0, v0
	s_movk_i32 s3, 0x60
	v_cmp_eq_u32_e32 vcc, s3, v43
	s_and_saveexec_b64 s[36:37], vcc
	v_lshlrev_b32_e32 v43, 4, v0
	v_and_b32_e32 v43, 0x180, v43
	v_and_b32_e32 v63, 7, v0
	s_lshl_b32 s38, s22, 3
	v_or3_b32 v43, s38, v43, v63
	v_lshlrev_b32_e32 v43, 2, v43
	global_load_dword v63, v43, s[10:11]
	global_load_dword v64, v43, s[8:9]
	global_load_dword v65, v43, s[26:27]
	s_mov_b64 exec, s[36:37]
	s_movk_i32 s3, 0x50
	v_bfe_u32 v1, v18, 8, 4
	v_cmp_gt_u32_e32 vcc, s3, v0
	s_and_saveexec_b64 s[6:7], vcc
	s_cbranch_execz .LBB0_17
	s_load_dwordx2 s[12:13], s[0:1], 0x18
	v_mul_u32_u24_e32 v2, 0x50, v1
	v_add_lshl_u32 v2, v2, v0, 2
	v_lshlrev_b32_e32 v3, 2, v0
	s_waitcnt lgkmcnt(0)
	s_waitcnt vmcnt(0)
	v_mov_b32_e32 v2, v62
	s_waitcnt vmcnt(0)
	ds_write_b32 v3, v2
.LBB0_17:
	s_or_b64 exec, exec, s[6:7]
	v_and_b32_e32 v2, 0xe0, v0
	s_movk_i32 s3, 0x60
	v_cmp_eq_u32_e32 vcc, s3, v2
	s_and_saveexec_b64 s[6:7], vcc
	s_cbranch_execz .LBB0_19
	v_lshlrev_b32_e32 v3, 4, v0
	v_and_b32_e32 v2, 7, v0
	v_and_b32_e32 v3, 0x180, v3
	s_waitcnt lgkmcnt(0)
	v_lshlrev_b32_e32 v4, 3, v1
	v_or3_b32 v2, v4, v3, v2
	v_lshlrev_b32_e32 v3, 2, v2
	s_waitcnt vmcnt(0)
	v_mov_b32_e32 v4, v63
	s_load_dwordx2 s[10:11], s[0:1], 0x10
	s_mov_b32 s12, 0x3fb8aa3b
	v_mov_b32_e32 v19, v64
	s_waitcnt lgkmcnt(0)
	v_mov_b32_e32 v20, v65
	s_mov_b32 s13, 0xc2ce8ed0
	s_mov_b32 s14, 0x42b17218
	v_mov_b32_e32 v16, 0x7f800000
	s_mov_b32 s15, 0x3f2aaaab
	v_mov_b32_e32 v12, 0x3ecc95a3
	v_mov_b32_e32 v2, 0x3f317218
	s_mov_b32 s18, 0x3f317218
	s_mov_b32 s3, 0x7f800000
	s_mov_b32 s19, 0x33800000
	v_and_b32_e32 v17, 31, v0
	s_waitcnt vmcnt(2)
	v_mul_f32_e32 v5, 0x3fb8aa3b, v4
	v_fma_f32 v6, v4, s12, -v5
	v_rndne_f32_e32 v7, v5
	v_fmamk_f32 v6, v4, 0x32a5705f, v6
	v_sub_f32_e32 v5, v5, v7
	v_add_f32_e32 v5, v5, v6
	v_cvt_i32_f32_e32 v7, v7
	v_exp_f32_e32 v5, v5
	v_cmp_ngt_f32_e32 vcc, s13, v4
	v_ldexp_f32 v3, v5, v7
	s_nop 0
	v_cndmask_b32_e32 v3, 0, v3, vcc
	v_cmp_nlt_f32_e32 vcc, s14, v4
	s_nop 1
	v_cndmask_b32_e32 v21, v16, v3, vcc
	v_add_f32_e32 v3, 1.0, v21
	v_add_f32_e32 v6, -1.0, v3
	v_frexp_mant_f32_e32 v7, v3
	v_cvt_f64_f32_e32 v[4:5], v3
	v_sub_f32_e32 v8, v6, v3
	v_frexp_exp_i32_f64_e32 v4, v[4:5]
	v_cmp_gt_f32_e32 vcc, s15, v7
	v_sub_f32_e32 v6, v21, v6
	v_add_f32_e32 v5, 1.0, v8
	v_subbrev_co_u32_e32 v4, vcc, 0, v4, vcc
	v_add_f32_e32 v5, v6, v5
	v_sub_u32_e32 v6, 0, v4
	v_ldexp_f32 v3, v3, v6
	v_ldexp_f32 v5, v5, v6
	v_add_f32_e32 v6, -1.0, v3
	v_add_f32_e32 v8, 1.0, v3
	v_add_f32_e32 v7, 1.0, v6
	v_add_f32_e32 v9, -1.0, v8
	v_sub_f32_e32 v7, v3, v7
	v_sub_f32_e32 v3, v3, v9
	v_add_f32_e32 v3, v5, v3
	v_add_f32_e32 v9, v5, v7
	v_add_f32_e32 v5, v8, v3
	v_rcp_f32_e32 v13, v5
	v_add_f32_e32 v7, v6, v9
	v_sub_f32_e32 v8, v8, v5
	v_add_f32_e32 v3, v3, v8
	v_mul_f32_e32 v15, v7, v13
	v_mul_f32_e32 v8, v5, v15
	v_fma_f32 v10, v15, v5, -v8
	v_sub_f32_e32 v6, v6, v7
	v_fmac_f32_e32 v10, v15, v3
	v_add_f32_e32 v14, v9, v6
	v_add_f32_e32 v6, v8, v10
	v_sub_f32_e32 v9, v7, v6
	v_mov_b32_e32 v11, v6
	v_pk_add_f32 v[6:7], v[6:7], v[8:9] neg_lo:[0,1] neg_hi:[0,1]
	v_cvt_f32_i32_e32 v4, v4
	v_pk_add_f32 v[6:7], v[6:7], v[10:11] neg_lo:[0,1] neg_hi:[0,1]
	v_cmp_neq_f32_e32 vcc, s3, v21
	v_add_f32_e32 v7, v14, v7
	v_add_f32_e32 v6, v6, v7
	v_add_f32_e32 v7, v9, v6
	v_mul_f32_e32 v11, v13, v7
	v_mul_f32_e32 v8, v5, v11
	v_fma_f32 v10, v11, v5, -v8
	v_sub_f32_e32 v9, v9, v7
	v_fmac_f32_e32 v10, v11, v3
	v_add_f32_e32 v14, v6, v9
	v_add_f32_e32 v22, v15, v11
	v_add_f32_e32 v6, v8, v10
	v_sub_f32_e32 v5, v22, v15
	v_sub_f32_e32 v9, v7, v6
	v_sub_f32_e32 v3, v11, v5
	v_mov_b32_e32 v11, v6
	v_pk_add_f32 v[6:7], v[6:7], v[8:9] neg_lo:[0,1] neg_hi:[0,1]
	s_nop 0
	v_pk_add_f32 v[6:7], v[6:7], v[10:11] neg_lo:[0,1] neg_hi:[0,1]
	s_nop 0
	v_add_f32_e32 v5, v14, v7
	v_add_f32_e32 v5, v6, v5
	v_add_f32_e32 v5, v9, v5
	v_mul_f32_e32 v5, v13, v5
	v_add_f32_e32 v3, v3, v5
	v_add_f32_e32 v5, v22, v3
	v_mul_f32_e32 v6, v5, v5
	v_sub_f32_e32 v8, v5, v22
	v_fmac_f32_e32 v12, 0x3e9b6dac, v6
	v_ldexp_f32 v7, v5, 1
	v_sub_f32_e32 v8, v3, v8
	v_mul_f32_e32 v5, v5, v6
	v_fmaak_f32 v3, v6, v12, 0x3f2aaada
	v_pk_mul_f32 v[2:3], v[4:5], v[2:3]
	v_ldexp_f32 v9, v8, 1
	v_fma_f32 v5, v4, s18, -v2
	v_fmamk_f32 v6, v4, 0xb102e308, v5
	v_pk_add_f32 v[4:5], v[2:3], v[6:7]
	v_mov_b32_e32 v8, v2
	v_sub_f32_e32 v12, v5, v7
	v_pk_add_f32 v[10:11], v[4:5], v[2:3] neg_lo:[0,1] neg_hi:[0,1]
	v_sub_f32_e32 v2, v3, v12
	v_add_f32_e32 v9, v9, v2
	v_pk_add_f32 v[2:3], v[4:5], v[8:9]
	v_mov_b32_e32 v7, v4
	v_mov_b32_e32 v11, v3
	v_pk_add_f32 v[14:15], v[6:7], v[10:11] neg_lo:[0,1] neg_hi:[0,1]
	v_pk_add_f32 v[6:7], v[6:7], v[10:11]
	v_mov_b32_e32 v13, v4
	v_pk_add_f32 v[10:11], v[6:7], v[4:5] op_sel:[1,0] op_sel_hi:[0,1] neg_lo:[0,1] neg_hi:[0,1]
	v_mov_b32_e32 v12, v9
	v_mov_b32_e32 v8, v3
	v_mov_b32_e32 v9, v7
	v_pk_mov_b32 v[4:5], v[4:5], v[10:11] op_sel:[1,0]
	v_pk_add_f32 v[2:3], v[2:3], v[10:11] op_sel_hi:[1,0] neg_lo:[0,1] neg_hi:[0,1]
	v_pk_add_f32 v[4:5], v[8:9], v[4:5] neg_lo:[0,1] neg_hi:[0,1]
	v_mov_b32_e32 v2, v14
	v_pk_add_f32 v[4:5], v[12:13], v[4:5] neg_lo:[0,1] neg_hi:[0,1]
	v_mov_b32_e32 v15, v7
	v_pk_add_f32 v[2:3], v[2:3], v[4:5]
	s_nop 0
	v_pk_add_f32 v[8:9], v[2:3], v[2:3] op_sel:[0,1] op_sel_hi:[1,0]
	s_nop 0
	v_pk_add_f32 v[6:7], v[6:7], v[8:9] op_sel:[1,0] op_sel_hi:[0,1]
	v_mov_b32_e32 v3, v6
	v_mov_b32_e32 v5, v8
	v_pk_add_f32 v[8:9], v[2:3], v[14:15] neg_lo:[0,1] neg_hi:[0,1]
	s_nop 0
	v_sub_f32_e32 v2, v2, v8
	v_pk_add_f32 v[4:5], v[4:5], v[8:9] neg_lo:[0,1] neg_hi:[0,1]
	v_sub_f32_e32 v2, v14, v2
	v_add_f32_e32 v2, v4, v2
	v_add_f32_e32 v2, v2, v5
	v_add_f32_e32 v2, v6, v2
	v_cndmask_b32_e32 v2, v16, v2, vcc
	v_cmp_lt_f32_e64 vcc, |v21|, s19
	s_nop 1
	v_cndmask_b32_e32 v2, v2, v21, vcc
	s_waitcnt vmcnt(0)
	v_fmac_f32_e32 v19, v20, v2
	v_lshlrev_b32_e32 v2, 2, v17
	ds_write_b32 v2, v19 offset:320

.LBB0_23:
	s_or_b64 exec, exec, s[6:7]
	s_waitcnt vmcnt(0)
	v_mov_b32_e32 v10, v56
	v_mov_b32_e32 v11, v57
	v_mov_b32_e32 v12, v58
	v_mov_b32_e32 v13, v59
	v_mov_b32_e32 v14, v52
	v_mov_b32_e32 v15, v53
	v_mov_b32_e32 v16, v54
	v_mov_b32_e32 v17, v55
	v_mov_b32_e32 v2, v48
	v_mov_b32_e32 v3, v49
	v_mov_b32_e32 v4, v50
	v_mov_b32_e32 v5, v51
	v_mov_b32_e32 v6, v44
	v_mov_b32_e32 v7, v45
	v_mov_b32_e32 v8, v46
	v_mov_b32_e32 v9, v47
	v_mov_b32_e32 v22, v60
	s_load_dwordx2 s[6:7], s[0:1], 0x58
	v_mov_b32_e32 v26, 0
	s_and_saveexec_b64 s[8:9], vcc
	s_cbranch_execz .LBB0_25
	v_mov_b32_e32 v26, v61

	.amdhsa_kernel _Z11prep_kernelPKfPDv8_DF16_S0_S0_S0_S0_S0_S0_S0_S0_S0_S2_PfPDF16_S4_S3_
		.amdhsa_group_segment_fixed_size 17440
		.amdhsa_private_segment_fixed_size 0
		.amdhsa_kernarg_size 128
		.amdhsa_user_sgpr_count 2
		.amdhsa_user_sgpr_dispatch_ptr 0
		.amdhsa_user_sgpr_queue_ptr 0
		.amdhsa_user_sgpr_kernarg_segment_ptr 1
		.amdhsa_user_sgpr_dispatch_id 0
		.amdhsa_user_sgpr_kernarg_preload_length 0
		.amdhsa_user_sgpr_kernarg_preload_offset 0
		.amdhsa_user_sgpr_private_segment_size 0
		.amdhsa_uses_dynamic_stack 0
		.amdhsa_enable_private_segment 0
		.amdhsa_system_sgpr_workgroup_id_x 1
		.amdhsa_system_sgpr_workgroup_id_y 0
		.amdhsa_system_sgpr_workgroup_id_z 0
		.amdhsa_system_sgpr_workgroup_info 0
		.amdhsa_system_vgpr_workitem_id 0
		.amdhsa_next_free_vgpr 66
		.amdhsa_next_free_sgpr 40
		.amdhsa_accum_offset 68
		.amdhsa_reserve_vcc 1
		.amdhsa_float_round_mode_32 0
		.amdhsa_float_round_mode_16_64 0
		.amdhsa_float_denorm_mode_32 3
		.amdhsa_float_denorm_mode_16_64 3
		.amdhsa_dx10_clamp 1
		.amdhsa_ieee_mode 1
		.amdhsa_fp16_overflow 0
		.amdhsa_tg_split 0
		.amdhsa_exception_fp_ieee_invalid_op 0
		.amdhsa_exception_fp_denorm_src 0
		.amdhsa_exception_fp_ieee_div_zero 0
		.amdhsa_exception_fp_ieee_overflow 0
		.amdhsa_exception_fp_ieee_underflow 0
		.amdhsa_exception_fp_ieee_inexact 0
		.amdhsa_exception_int_div_zero 0
	.end_amdhsa_kernel

amdhsa.kernels:
  - .agpr_count:     0
    .args:
      - .actual_access:  read_only
        .address_space:  global
        .offset:         0
        .size:           8
        .value_kind:     global_buffer
      - .actual_access:  write_only
        .address_space:  global
        .offset:         8
        .size:           8
        .value_kind:     global_buffer
      - .actual_access:  read_only
        .address_space:  global
        .offset:         16
        .size:           8
        .value_kind:     global_buffer
      - .actual_access:  read_only
        .address_space:  global
        .offset:         24
        .size:           8
        .value_kind:     global_buffer
      - .actual_access:  read_only
        .address_space:  global
        .offset:         32
        .size:           8
        .value_kind:     global_buffer
      - .actual_access:  read_only
        .address_space:  global
        .offset:         40
        .size:           8
        .value_kind:     global_buffer
      - .actual_access:  read_only
        .address_space:  global
        .offset:         48
        .size:           8
        .value_kind:     global_buffer
      - .actual_access:  read_only
        .address_space:  global
        .offset:         56
        .size:           8
        .value_kind:     global_buffer
      - .actual_access:  read_only
        .address_space:  global
        .offset:         64
        .size:           8
        .value_kind:     global_buffer
      - .actual_access:  read_only
        .address_space:  global
        .offset:         72
        .size:           8
        .value_kind:     global_buffer
      - .actual_access:  read_only
        .address_space:  global
        .offset:         80
        .size:           8
        .value_kind:     global_buffer
      - .actual_access:  write_only
        .address_space:  global
        .offset:         88
        .size:           8
        .value_kind:     global_buffer
      - .actual_access:  write_only
        .address_space:  global
        .offset:         96
        .size:           8
        .value_kind:     global_buffer
      - .actual_access:  write_only
        .address_space:  global
        .offset:         104
        .size:           8
        .value_kind:     global_buffer
      - .actual_access:  write_only
        .address_space:  global
        .offset:         112
        .size:           8
        .value_kind:     global_buffer
      - .actual_access:  write_only
        .address_space:  global
        .offset:         120
        .size:           8
        .value_kind:     global_buffer
    .group_segment_fixed_size: 17440
    .kernarg_segment_align: 8
    .kernarg_segment_size: 128
    .language:       OpenCL C
    .language_version:
      - 2
      - 0
    .max_flat_workgroup_size: 256
    .name:           _Z11prep_kernelPKfPDv8_DF16_S0_S0_S0_S0_S0_S0_S0_S0_S0_S2_PfPDF16_S4_S3_
    .private_segment_fixed_size: 0
    .sgpr_count:     46
    .sgpr_spill_count: 0
    .symbol:         _Z11prep_kernelPKfPDv8_DF16_S0_S0_S0_S0_S0_S0_S0_S0_S0_S2_PfPDF16_S4_S3_.kd
    .uniform_work_group_size: 1
    .uses_dynamic_stack: false
    .vgpr_count:     66
    .vgpr_spill_count: 0
    .wavefront_size: 64
  - .agpr_count:     0
    .args:
      - .actual_access:  read_only
        .address_space:  global
        .offset:         0
        .size:           8
        .value_kind:     global_buffer
      - .actual_access:  read_only
        .address_space:  global
        .offset:         8
        .size:           8
        .value_kind:     global_buffer
      - .actual_access:  read_only
        .address_space:  global
        .offset:         16
        .size:           8
        .value_kind:     global_buffer
      - .actual_access:  read_only
        .address_space:  global
        .offset:         24
        .size:           8
        .value_kind:     global_buffer
      - .actual_access:  read_only
        .address_space:  global
        .offset:         32
        .size:           8
        .value_kind:     global_buffer
      - .actual_access:  read_only
        .address_space:  global
        .offset:         40
        .size:           8
        .value_kind:     global_buffer
      - .actual_access:  read_only
        .address_space:  global
        .offset:         48
        .size:           8
        .value_kind:     global_buffer
      - .actual_access:  read_only
        .address_space:  global
        .offset:         56
        .size:           8
        .value_kind:     global_buffer
      - .actual_access:  read_only
        .address_space:  global
        .offset:         64
        .size:           8
        .value_kind:     global_buffer
      - .actual_access:  write_only
        .address_space:  global
        .offset:         72
        .size:           8
        .value_kind:     global_buffer
    .group_segment_fixed_size: 130304
    .kernarg_segment_align: 8
    .kernarg_segment_size: 80
    .language:       OpenCL C
    .language_version:
      - 2
      - 0
    .max_flat_workgroup_size: 512
    .name:           _Z16pdag_main_kernelPKfS0_S0_PKDv8_DF16_S3_S0_PKDF16_S5_S0_Pf
    .private_segment_fixed_size: 0
    .sgpr_count:     92
    .sgpr_spill_count: 0
    .symbol:         _Z16pdag_main_kernelPKfS0_S0_PKDv8_DF16_S3_S0_PKDF16_S5_S0_Pf.kd
    .uniform_work_group_size: 1
    .uses_dynamic_stack: false
    .vgpr_count:     256
    .vgpr_spill_count: 0
    .wavefront_size: 64
